# unscaled fp8 MFMA form plus merge-epilogue loop: next-row loads stay in flight during the current row's math (wait moved to the register copies)
# speedup vs baseline: 1.0046x; 1.0046x over previous
; __device__ __forceinline__ unsigned cvt_pk_bf16(float lo, float hi) { unsigned r; asm volatile("v_cvt_pk_bf16_f32 %0, %1, %2" : "=v"(r) : "v"(lo), "v"(hi)); return r; }
; __device__ __forceinline__ float bf_lo(unsigned w) { return __uint_as_float(w << 16); }
; __device__ __forceinline__ float bf_hi(unsigned w) { return __uint_as_float(w & 0xffff0000u); }
; template <int QS, int KS, int OS, bool SEL, int QREG, bool MERGE>
; __device__ __forceinline__ void attn_block(const BlockRef& cur, const BlockRef& nxt, int skv, int W, char* lds, Seam& S, const MergeArgs& MG, const int wid) {
;     ...
;             for (int p = 0; p < 8; ++p) {
;                 const int row = 4 * p + rq;
;                 const size_t e = eoff + (size_t)row * OS;
;                 const u32x4 y = *(const u32x4*)(stg + row * 256 + ch * 16);
;                 if (p < 7) MG_LOAD(p + 1, na, nga, np2, np1, np0);
;                 float ov[8];
; #pragma unroll
;                 for (int j = 0; j < 4; ++j) {
;                     ov[2 * j] = bf_lo(ca[j]) * (w0[2 * j] * bf_lo(cp0[j]) + w1[2 * j] * bf_lo(cp1[j]) + w2[2 * j] * bf_lo(cp2[j])) + bf_lo(cga[j]) * bf_lo(y[j]);
;                     ov[2 * j + 1] = bf_hi(ca[j]) * (w0[2 * j + 1] * bf_hi(cp0[j]) + w1[2 * j + 1] * bf_hi(cp1[j]) + w2[2 * j + 1] * bf_hi(cp2[j])) + bf_hi(cga[j]) * bf_hi(y[j]);
;                 }
;                 u32x4 wv_; wv_.x = cvt_pk_bf16(ov[0], ov[1]); wv_.y = cvt_pk_bf16(ov[2], ov[3]); wv_.z = cvt_pk_bf16(ov[4], ov[5]); wv_.w = cvt_pk_bf16(ov[6], ov[7]);
;                 *(u32x4*)(MOUT + e) = wv_;
;                 ca = na; cga = nga; cp2 = np2; cp1 = np1; cp0 = np0;
;             }
.LBB0_1968:
	s_cmp_lg_u32 s0, 0
	s_cbranch_scc1 .Lmg_nowait
	s_waitcnt vmcnt(0)
.Lmg_nowait:
	v_lshlrev_b32_e32 v2, 16, v52
	v_lshlrev_b32_e32 v3, 16, v44
	v_lshlrev_b32_e32 v0, 16, v48
	v_pk_mul_f32 v[2:3], v[16:17], v[2:3]
	s_waitcnt lgkmcnt(0)
	v_lshlrev_b32_e32 v87, 16, v76
	v_fma_f32 v0, v20, v0, v2
	v_add_f32_e32 v2, v0, v3
	v_lshlrev_b32_e32 v3, 16, v40
	v_lshlrev_b32_e32 v86, 16, v36
	v_pk_mul_f32 v[2:3], v[2:3], v[86:87]
	v_and_b32_e32 v48, 0xffff0000, v48
	v_add_f32_e32 v0, v2, v3
	v_and_b32_e32 v3, 0xffff0000, v44
	v_and_b32_e32 v2, 0xffff0000, v52
	v_pk_mul_f32 v[2:3], v[28:29], v[2:3]
	v_and_b32_e32 v87, 0xffff0000, v76
	v_fma_f32 v2, v21, v48, v2
	v_add_f32_e32 v2, v2, v3
	v_and_b32_e32 v3, 0xffff0000, v40
	v_and_b32_e32 v86, 0xffff0000, v36
	v_pk_mul_f32 v[2:3], v[2:3], v[86:87]
	v_lshlrev_b32_e32 v36, 16, v49
	v_add_f32_e32 v44, v2, v3
	v_lshlrev_b32_e32 v2, 16, v53
	v_lshlrev_b32_e32 v3, 16, v45
	v_pk_mul_f32 v[2:3], v[18:19], v[2:3]
	v_lshlrev_b32_e32 v87, 16, v77
	v_fma_f32 v2, v22, v36, v2
	v_add_f32_e32 v2, v2, v3
	v_lshlrev_b32_e32 v3, 16, v41
	v_lshlrev_b32_e32 v86, 16, v37
	v_pk_mul_f32 v[2:3], v[2:3], v[86:87]
	v_and_b32_e32 v36, 0xffff0000, v49
	v_add_f32_e32 v48, v2, v3
	v_and_b32_e32 v3, 0xffff0000, v45
	v_and_b32_e32 v2, 0xffff0000, v53
	v_pk_mul_f32 v[2:3], v[30:31], v[2:3]
	v_and_b32_e32 v40, 0xffff0000, v37
	v_fma_f32 v2, v23, v36, v2
	v_add_f32_e32 v2, v2, v3
	v_and_b32_e32 v3, 0xffff0000, v41
	v_and_b32_e32 v41, 0xffff0000, v77
	v_pk_mul_f32 v[2:3], v[2:3], v[40:41]
	v_lshlrev_b32_e32 v36, 16, v50
	v_add_f32_e32 v40, v2, v3
	v_lshlrev_b32_e32 v2, 16, v54
	v_lshlrev_b32_e32 v3, 16, v46
	v_pk_mul_f32 v[2:3], v[12:13], v[2:3]
	v_lshlrev_b32_e32 v37, 16, v78
	v_fma_f32 v2, v24, v36, v2
	v_add_f32_e32 v2, v2, v3
	v_lshlrev_b32_e32 v3, 16, v42
	v_lshlrev_b32_e32 v36, 16, v38
	v_pk_mul_f32 v[2:3], v[2:3], v[36:37]
	v_and_b32_e32 v36, 0xffff0000, v50
	v_add_f32_e32 v41, v2, v3
	v_and_b32_e32 v3, 0xffff0000, v46
	v_and_b32_e32 v2, 0xffff0000, v54
	v_pk_mul_f32 v[2:3], v[32:33], v[2:3]
	v_and_b32_e32 v37, 0xffff0000, v78
	v_fma_f32 v2, v25, v36, v2
	v_add_f32_e32 v2, v2, v3
	v_and_b32_e32 v3, 0xffff0000, v42
	v_and_b32_e32 v36, 0xffff0000, v38
	v_pk_mul_f32 v[2:3], v[2:3], v[36:37]
	v_lshlrev_b32_e32 v36, 16, v51
	v_add_f32_e32 v38, v2, v3
	v_lshlrev_b32_e32 v2, 16, v55
	v_lshlrev_b32_e32 v3, 16, v47
	v_pk_mul_f32 v[2:3], v[14:15], v[2:3]
	v_lshlrev_b32_e32 v37, 16, v79
	v_fma_f32 v2, v26, v36, v2
	v_add_f32_e32 v2, v2, v3
	v_lshlrev_b32_e32 v3, 16, v43
	v_lshlrev_b32_e32 v36, 16, v39
	v_pk_mul_f32 v[2:3], v[2:3], v[36:37]
	v_and_b32_e32 v36, 0xffff0000, v51
	v_add_f32_e32 v42, v2, v3
	v_and_b32_e32 v3, 0xffff0000, v47
	v_and_b32_e32 v2, 0xffff0000, v55
	v_pk_mul_f32 v[2:3], v[34:35], v[2:3]
	v_and_b32_e32 v37, 0xffff0000, v79
	v_fma_f32 v2, v27, v36, v2
	v_add_f32_e32 v2, v2, v3
	v_and_b32_e32 v3, 0xffff0000, v43
	v_and_b32_e32 v36, 0xffff0000, v39
	v_pk_mul_f32 v[2:3], v[2:3], v[36:37]
	v_cvt_pk_bf16_f32 v36, v0, v44
	v_cvt_pk_bf16_f32 v37, v48, v40
	v_cvt_pk_bf16_f32 v38, v41, v38
	s_add_u32 s0, s0, 0x4000
	v_add_f32_e32 v2, v2, v3
	v_cvt_pk_bf16_f32 v39, v42, v2
	v_add_co_u32_e32 v2, vcc, s83, v82
	s_addc_u32 s1, s1, 0
	s_nop 0
	v_addc_co_u32_e32 v3, vcc, 0, v83, vcc
	global_store_dwordx4 v[2:3], v[36:39], off
	s_waitcnt vmcnt(1)
	v_mov_b64_e32 v[48:49], v[68:69]
	v_mov_b64_e32 v[44:45], v[64:65]
	v_mov_b64_e32 v[40:41], v[60:61]
	v_mov_b64_e32 v[36:37], v[56:57]
	v_add_u32_e32 v84, 4, v84
	v_add_u32_e32 v85, 0x400, v85
	s_cmp_lg_u32 s0, 0x20000
	v_mov_b64_e32 v[50:51], v[70:71]
	v_mov_b64_e32 v[46:47], v[66:67]
	v_mov_b64_e32 v[42:43], v[62:63]
	v_mov_b64_e32 v[38:39], v[58:59]
	v_mov_b32_e32 v52, v72
	v_mov_b32_e32 v53, v73
	v_mov_b32_e32 v54, v74
	v_mov_b32_e32 v55, v75
	s_cbranch_scc0 .LBB0_1790
